# P0 weight-transpose work queue: waves claim 4 items per atomic instead of 8 (items spread over twice as many waves)
# baseline (speedup 1.0000x reference)
; #define RI_NEXT(D_) do { if (q.cnt == 8) { int b_ = 0; if (F.lane == 0) b_ = (int)__hip_atomic_fetch_add(qctr, 8u, __ATOMIC_RELAXED, __HIP_MEMORY_SCOPE_AGENT); q.base = __builtin_amdgcn_readfirstlane(b_); q.cnt = 0; } \
;         D_ = decode_item(KA, F.ws, kind, q.base + q.cnt); ++q.cnt; } while (0)
; DI void run_items1(Frame& F, int kind, int quota, QState& q) {
;     ...
;     if (quota == 0) return;
;     TItem d; RI_NEXT(d); if (!d.valid) return;
.LBB0_79:
	s_mov_b32 s2, -1
	s_add_u32 s0, s46, 0x8000
	v_mbcnt_lo_u32_b32 v1, s2, 0
	v_mbcnt_hi_u32_b32 v64, s2, v1
	s_mov_b32 s2, s88
	s_addc_u32 s1, s47, 0
	v_mov_b32_e32 v0, 0
	s_mov_b64 s[2:3], s[70:71]
	v_cmp_eq_u32_e64 s[4:5], 0, v64
	s_and_saveexec_b64 s[6:7], s[4:5]
	s_cbranch_execz .LBB0_83
	s_mov_b64 s[10:11], exec
	v_mbcnt_lo_u32_b32 v0, s10, 0
	v_mbcnt_hi_u32_b32 v0, s11, v0
	v_cmp_eq_u32_e32 vcc, 0, v0
	s_and_saveexec_b64 s[8:9], vcc
	s_cbranch_execz .LBB0_82
	s_bcnt1_i32_b64 s10, s[10:11]
	s_lshl_b32 s10, s10, 2
	v_mov_b32_e32 v1, 0
	v_mov_b32_e32 v2, s10
	global_atomic_add v1, v1, v2, s[0:1] sc0
.LBB0_82:
	s_or_b64 exec, exec, s[8:9]
	s_waitcnt vmcnt(0)
	v_readfirstlane_b32 s8, v1
	s_nop 1
	v_lshl_add_u32 v0, v0, 2, s8

; #define LDS_WAIT() asm volatile("s_waitcnt lgkmcnt(0)" ::: "memory")
; DI void item_scatter(const f32x4 (&v)[16], LAS float* scr, int lane) {
;     ...
;     for (int i = 0; i < 16; ++i) { const int k = 4 * i + r4;
; #pragma unroll
;         for (int j = 0; j < 4; ++j) scr[(4 * c4 + j) * 64 + (k ^ (4 * (c4 ^ j)))] = v[i][j]; }
;     LDS_WAIT(); asm volatile("" ::: "memory");
.LBB0_95:
	s_waitcnt vmcnt(0)
	ds_write_b32 v72, v24
	ds_write_b32 v73, v25 offset:256
	ds_write_b32 v74, v26 offset:512
	ds_write_b32 v75, v27 offset:768
	ds_write_b32 v76, v0
	ds_write_b32 v77, v1 offset:256
	ds_write_b32 v78, v2 offset:512
	ds_write_b32 v79, v3 offset:768
	ds_write_b32 v80, v4
	ds_write_b32 v81, v5 offset:256
	ds_write_b32 v82, v6 offset:512
	ds_write_b32 v83, v7 offset:768
	ds_write_b32 v84, v8
	ds_write_b32 v85, v9 offset:256
	ds_write_b32 v86, v10 offset:512
	ds_write_b32 v87, v11 offset:768
	ds_write_b32 v88, v12
	ds_write_b32 v89, v13 offset:256
	ds_write_b32 v90, v14 offset:512
	ds_write_b32 v91, v15 offset:768
	ds_write_b32 v92, v16
	ds_write_b32 v93, v17 offset:256
	ds_write_b32 v94, v18 offset:512
	ds_write_b32 v95, v19 offset:768
	ds_write_b32 v96, v20
	ds_write_b32 v97, v21 offset:256
	ds_write_b32 v98, v22 offset:512
	ds_write_b32 v99, v23 offset:768
	ds_write_b32 v100, v28
	ds_write_b32 v101, v29 offset:256
	ds_write_b32 v102, v30 offset:512
	ds_write_b32 v103, v31 offset:768
	ds_write_b32 v104, v32
	ds_write_b32 v105, v33 offset:256
	ds_write_b32 v106, v34 offset:512
	ds_write_b32 v107, v35 offset:768
	ds_write_b32 v108, v36
	ds_write_b32 v109, v37 offset:256
	ds_write_b32 v110, v38 offset:512
	ds_write_b32 v111, v39 offset:768
	ds_write_b32 v112, v40
	ds_write_b32 v113, v41 offset:256
	ds_write_b32 v114, v42 offset:512
	ds_write_b32 v115, v43 offset:768
	ds_write_b32 v116, v44
	ds_write_b32 v117, v45 offset:256
	ds_write_b32 v118, v46 offset:512
	ds_write_b32 v119, v47 offset:768
	ds_write_b32 v120, v48
	ds_write_b32 v121, v49 offset:256
	ds_write_b32 v122, v50 offset:512
	ds_write_b32 v123, v51 offset:768
	ds_write_b32 v124, v52
	ds_write_b32 v125, v53 offset:256
	ds_write_b32 v126, v54 offset:512
	ds_write_b32 v127, v55 offset:768
	ds_write_b32 v128, v56
	ds_write_b32 v129, v57 offset:256
	ds_write_b32 v130, v58 offset:512
	ds_write_b32 v131, v59 offset:768
	ds_write_b32 v132, v60
	ds_write_b32 v133, v61 offset:256
	ds_write_b32 v134, v62 offset:512
	ds_write_b32 v135, v63 offset:768
	s_waitcnt lgkmcnt(0)
	s_cmp_lg_u32 s31, 4
	s_cbranch_scc1 .LBB0_101
	v_mov_b32_e32 v64, 0
	s_and_saveexec_b64 s[14:15], s[4:5]
	s_cbranch_execz .LBB0_100
	s_mov_b64 s[18:19], exec
	v_mbcnt_lo_u32_b32 v64, s18, 0
	v_mbcnt_hi_u32_b32 v64, s19, v64
	v_cmp_eq_u32_e32 vcc, 0, v64
	s_and_saveexec_b64 s[16:17], vcc
	s_cbranch_execz .LBB0_99
	s_bcnt1_i32_b64 s18, s[18:19]
	s_lshl_b32 s18, s18, 2
	v_mov_b32_e32 v65, s18
	global_atomic_add v65, v69, v65, s[0:1] sc0
.LBB0_99:
	s_or_b64 exec, exec, s[16:17]
	s_waitcnt vmcnt(0)
	v_readfirstlane_b32 s16, v65
	s_nop 1
	v_lshl_add_u32 v64, v64, 2, s16
